# speedup vs baseline: 1.0091x; 1.0091x over previous
.LBB2_62:
	v_subrev_u32_e32 v10, s10, v16
	v_sub_u32_e32 v11, v17, v16
	v_lshlrev_b32_e32 v10, 2, v10
	v_lshlrev_b32_e32 v9, 4, v23
	s_mov_b64 s[16:17], exec
	v_cmp_le_u32_e32 vcc, 8, v11
	s_mov_b64 s[12:13], vcc
	s_mov_b64 exec, vcc
	s_cbranch_execz .Lk3_drainA
	ds_read2_b32 v[12:13], v10 offset1:1
	ds_read2_b32 v[14:15], v10 offset0:2 offset1:3
	ds_read2_b32 v[16:17], v10 offset0:4 offset1:5
	ds_read2_b32 v[18:19], v10 offset0:6 offset1:7
	v_add_u32_e32 v10, 32, v10
	v_subrev_u32_e32 v11, 8, v11
	s_waitcnt lgkmcnt(0)
	v_lshl_or_b32 v12, v12, 5, v9
	v_lshl_or_b32 v13, v13, 5, v9
	v_lshl_or_b32 v14, v14, 5, v9
	v_lshl_or_b32 v15, v15, 5, v9
	v_lshl_or_b32 v16, v16, 5, v9
	v_lshl_or_b32 v17, v17, 5, v9
	v_lshl_or_b32 v18, v18, 5, v9
	v_lshl_or_b32 v19, v19, 5, v9
	global_load_dwordx4 v[32:35], v12, s[8:9]
	global_load_dwordx4 v[36:39], v13, s[8:9]
	global_load_dwordx4 v[40:43], v14, s[8:9]
	global_load_dwordx4 v[44:47], v15, s[8:9]
	global_load_dwordx4 v[48:51], v16, s[8:9]
	global_load_dwordx4 v[52:55], v17, s[8:9]
	global_load_dwordx4 v[56:59], v18, s[8:9]
	global_load_dwordx4 v[60:63], v19, s[8:9]
.Lk3_loop:
	v_cmp_le_u32_e32 vcc, 8, v11
	s_mov_b64 s[14:15], vcc
	s_mov_b64 exec, vcc
	s_cbranch_execz .Lk3_drainA
	ds_read2_b32 v[12:13], v10 offset1:1
	ds_read2_b32 v[14:15], v10 offset0:2 offset1:3
	ds_read2_b32 v[16:17], v10 offset0:4 offset1:5
	ds_read2_b32 v[18:19], v10 offset0:6 offset1:7
	v_add_u32_e32 v10, 32, v10
	v_subrev_u32_e32 v11, 8, v11
	s_waitcnt lgkmcnt(0)
	v_lshl_or_b32 v12, v12, 5, v9
	v_lshl_or_b32 v13, v13, 5, v9
	v_lshl_or_b32 v14, v14, 5, v9
	v_lshl_or_b32 v15, v15, 5, v9
	v_lshl_or_b32 v16, v16, 5, v9
	v_lshl_or_b32 v17, v17, 5, v9
	v_lshl_or_b32 v18, v18, 5, v9
	v_lshl_or_b32 v19, v19, 5, v9
	global_load_dwordx4 v[64:67], v12, s[8:9]
	global_load_dwordx4 v[68:71], v13, s[8:9]
	global_load_dwordx4 v[72:75], v14, s[8:9]
	global_load_dwordx4 v[76:79], v15, s[8:9]
	global_load_dwordx4 v[80:83], v16, s[8:9]
	global_load_dwordx4 v[84:87], v17, s[8:9]
	global_load_dwordx4 v[88:91], v18, s[8:9]
	global_load_dwordx4 v[92:95], v19, s[8:9]
	s_mov_b64 exec, s[12:13]
	s_waitcnt vmcnt(14)
	v_pk_add_f16 v32, v32, v36
	v_pk_add_f16 v33, v33, v37
	v_pk_add_f16 v34, v34, v38
	v_pk_add_f16 v35, v35, v39
	v_fma_mix_f32 v0, v32, 1.0, v0 op_sel_hi:[1,0,0]
	v_fma_mix_f32 v1, v32, 1.0, v1 op_sel:[1,0,0] op_sel_hi:[1,0,0]
	v_fma_mix_f32 v2, v33, 1.0, v2 op_sel_hi:[1,0,0]
	v_fma_mix_f32 v3, v33, 1.0, v3 op_sel:[1,0,0] op_sel_hi:[1,0,0]
	v_fma_mix_f32 v4, v34, 1.0, v4 op_sel_hi:[1,0,0]
	v_fma_mix_f32 v5, v34, 1.0, v5 op_sel:[1,0,0] op_sel_hi:[1,0,0]
	v_fma_mix_f32 v6, v35, 1.0, v6 op_sel_hi:[1,0,0]
	v_fma_mix_f32 v7, v35, 1.0, v7 op_sel:[1,0,0] op_sel_hi:[1,0,0]
	s_waitcnt vmcnt(12)
	v_pk_add_f16 v40, v40, v44
	v_pk_add_f16 v41, v41, v45
	v_pk_add_f16 v42, v42, v46
	v_pk_add_f16 v43, v43, v47
	v_fma_mix_f32 v0, v40, 1.0, v0 op_sel_hi:[1,0,0]
	v_fma_mix_f32 v1, v40, 1.0, v1 op_sel:[1,0,0] op_sel_hi:[1,0,0]
	v_fma_mix_f32 v2, v41, 1.0, v2 op_sel_hi:[1,0,0]
	v_fma_mix_f32 v3, v41, 1.0, v3 op_sel:[1,0,0] op_sel_hi:[1,0,0]
	v_fma_mix_f32 v4, v42, 1.0, v4 op_sel_hi:[1,0,0]
	v_fma_mix_f32 v5, v42, 1.0, v5 op_sel:[1,0,0] op_sel_hi:[1,0,0]
	v_fma_mix_f32 v6, v43, 1.0, v6 op_sel_hi:[1,0,0]
	v_fma_mix_f32 v7, v43, 1.0, v7 op_sel:[1,0,0] op_sel_hi:[1,0,0]
	s_waitcnt vmcnt(10)
	v_pk_add_f16 v48, v48, v52
	v_pk_add_f16 v49, v49, v53
	v_pk_add_f16 v50, v50, v54
	v_pk_add_f16 v51, v51, v55
	v_fma_mix_f32 v0, v48, 1.0, v0 op_sel_hi:[1,0,0]
	v_fma_mix_f32 v1, v48, 1.0, v1 op_sel:[1,0,0] op_sel_hi:[1,0,0]
	v_fma_mix_f32 v2, v49, 1.0, v2 op_sel_hi:[1,0,0]
	v_fma_mix_f32 v3, v49, 1.0, v3 op_sel:[1,0,0] op_sel_hi:[1,0,0]
	v_fma_mix_f32 v4, v50, 1.0, v4 op_sel_hi:[1,0,0]
	v_fma_mix_f32 v5, v50, 1.0, v5 op_sel:[1,0,0] op_sel_hi:[1,0,0]
	v_fma_mix_f32 v6, v51, 1.0, v6 op_sel_hi:[1,0,0]
	v_fma_mix_f32 v7, v51, 1.0, v7 op_sel:[1,0,0] op_sel_hi:[1,0,0]
	s_waitcnt vmcnt(8)
	v_pk_add_f16 v56, v56, v60
	v_pk_add_f16 v57, v57, v61
	v_pk_add_f16 v58, v58, v62
	v_pk_add_f16 v59, v59, v63
	v_fma_mix_f32 v0, v56, 1.0, v0 op_sel_hi:[1,0,0]
	v_fma_mix_f32 v1, v56, 1.0, v1 op_sel:[1,0,0] op_sel_hi:[1,0,0]
	v_fma_mix_f32 v2, v57, 1.0, v2 op_sel_hi:[1,0,0]
	v_fma_mix_f32 v3, v57, 1.0, v3 op_sel:[1,0,0] op_sel_hi:[1,0,0]
	v_fma_mix_f32 v4, v58, 1.0, v4 op_sel_hi:[1,0,0]
	v_fma_mix_f32 v5, v58, 1.0, v5 op_sel:[1,0,0] op_sel_hi:[1,0,0]
	v_fma_mix_f32 v6, v59, 1.0, v6 op_sel_hi:[1,0,0]
	v_fma_mix_f32 v7, v59, 1.0, v7 op_sel:[1,0,0] op_sel_hi:[1,0,0]
	s_mov_b64 exec, s[14:15]
	v_cmp_le_u32_e32 vcc, 8, v11
	s_mov_b64 s[12:13], vcc
	s_mov_b64 exec, vcc
	s_cbranch_execz .Lk3_drainB
	ds_read2_b32 v[12:13], v10 offset1:1
	ds_read2_b32 v[14:15], v10 offset0:2 offset1:3
	ds_read2_b32 v[16:17], v10 offset0:4 offset1:5
	ds_read2_b32 v[18:19], v10 offset0:6 offset1:7
	v_add_u32_e32 v10, 32, v10
	v_subrev_u32_e32 v11, 8, v11
	s_waitcnt lgkmcnt(0)
	v_lshl_or_b32 v12, v12, 5, v9
	v_lshl_or_b32 v13, v13, 5, v9
	v_lshl_or_b32 v14, v14, 5, v9
	v_lshl_or_b32 v15, v15, 5, v9
	v_lshl_or_b32 v16, v16, 5, v9
	v_lshl_or_b32 v17, v17, 5, v9
	v_lshl_or_b32 v18, v18, 5, v9
	v_lshl_or_b32 v19, v19, 5, v9
	global_load_dwordx4 v[32:35], v12, s[8:9]
	global_load_dwordx4 v[36:39], v13, s[8:9]
	global_load_dwordx4 v[40:43], v14, s[8:9]
	global_load_dwordx4 v[44:47], v15, s[8:9]
	global_load_dwordx4 v[48:51], v16, s[8:9]
	global_load_dwordx4 v[52:55], v17, s[8:9]
	global_load_dwordx4 v[56:59], v18, s[8:9]
	global_load_dwordx4 v[60:63], v19, s[8:9]
	s_mov_b64 exec, s[14:15]
	s_waitcnt vmcnt(14)
	v_pk_add_f16 v64, v64, v68
	v_pk_add_f16 v65, v65, v69
	v_pk_add_f16 v66, v66, v70
	v_pk_add_f16 v67, v67, v71
	v_fma_mix_f32 v0, v64, 1.0, v0 op_sel_hi:[1,0,0]
	v_fma_mix_f32 v1, v64, 1.0, v1 op_sel:[1,0,0] op_sel_hi:[1,0,0]
	v_fma_mix_f32 v2, v65, 1.0, v2 op_sel_hi:[1,0,0]
	v_fma_mix_f32 v3, v65, 1.0, v3 op_sel:[1,0,0] op_sel_hi:[1,0,0]
	v_fma_mix_f32 v4, v66, 1.0, v4 op_sel_hi:[1,0,0]
	v_fma_mix_f32 v5, v66, 1.0, v5 op_sel:[1,0,0] op_sel_hi:[1,0,0]
	v_fma_mix_f32 v6, v67, 1.0, v6 op_sel_hi:[1,0,0]
	v_fma_mix_f32 v7, v67, 1.0, v7 op_sel:[1,0,0] op_sel_hi:[1,0,0]
	s_waitcnt vmcnt(12)
	v_pk_add_f16 v72, v72, v76
	v_pk_add_f16 v73, v73, v77
	v_pk_add_f16 v74, v74, v78
	v_pk_add_f16 v75, v75, v79
	v_fma_mix_f32 v0, v72, 1.0, v0 op_sel_hi:[1,0,0]
	v_fma_mix_f32 v1, v72, 1.0, v1 op_sel:[1,0,0] op_sel_hi:[1,0,0]
	v_fma_mix_f32 v2, v73, 1.0, v2 op_sel_hi:[1,0,0]
	v_fma_mix_f32 v3, v73, 1.0, v3 op_sel:[1,0,0] op_sel_hi:[1,0,0]
	v_fma_mix_f32 v4, v74, 1.0, v4 op_sel_hi:[1,0,0]
	v_fma_mix_f32 v5, v74, 1.0, v5 op_sel:[1,0,0] op_sel_hi:[1,0,0]
	v_fma_mix_f32 v6, v75, 1.0, v6 op_sel_hi:[1,0,0]
	v_fma_mix_f32 v7, v75, 1.0, v7 op_sel:[1,0,0] op_sel_hi:[1,0,0]
	s_waitcnt vmcnt(10)
	v_pk_add_f16 v80, v80, v84
	v_pk_add_f16 v81, v81, v85
	v_pk_add_f16 v82, v82, v86
	v_pk_add_f16 v83, v83, v87
	v_fma_mix_f32 v0, v80, 1.0, v0 op_sel_hi:[1,0,0]
	v_fma_mix_f32 v1, v80, 1.0, v1 op_sel:[1,0,0] op_sel_hi:[1,0,0]
	v_fma_mix_f32 v2, v81, 1.0, v2 op_sel_hi:[1,0,0]
	v_fma_mix_f32 v3, v81, 1.0, v3 op_sel:[1,0,0] op_sel_hi:[1,0,0]
	v_fma_mix_f32 v4, v82, 1.0, v4 op_sel_hi:[1,0,0]
	v_fma_mix_f32 v5, v82, 1.0, v5 op_sel:[1,0,0] op_sel_hi:[1,0,0]
	v_fma_mix_f32 v6, v83, 1.0, v6 op_sel_hi:[1,0,0]
	v_fma_mix_f32 v7, v83, 1.0, v7 op_sel:[1,0,0] op_sel_hi:[1,0,0]
	s_waitcnt vmcnt(8)
	v_pk_add_f16 v88, v88, v92
	v_pk_add_f16 v89, v89, v93
	v_pk_add_f16 v90, v90, v94
	v_pk_add_f16 v91, v91, v95
	v_fma_mix_f32 v0, v88, 1.0, v0 op_sel_hi:[1,0,0]
	v_fma_mix_f32 v1, v88, 1.0, v1 op_sel:[1,0,0] op_sel_hi:[1,0,0]
	v_fma_mix_f32 v2, v89, 1.0, v2 op_sel_hi:[1,0,0]
	v_fma_mix_f32 v3, v89, 1.0, v3 op_sel:[1,0,0] op_sel_hi:[1,0,0]
	v_fma_mix_f32 v4, v90, 1.0, v4 op_sel_hi:[1,0,0]
	v_fma_mix_f32 v5, v90, 1.0, v5 op_sel:[1,0,0] op_sel_hi:[1,0,0]
	v_fma_mix_f32 v6, v91, 1.0, v6 op_sel_hi:[1,0,0]
	v_fma_mix_f32 v7, v91, 1.0, v7 op_sel:[1,0,0] op_sel_hi:[1,0,0]
	s_mov_b64 exec, s[12:13]
	s_branch .Lk3_loop
.Lk3_drainA:
	s_mov_b64 exec, s[16:17]
	v_cmp_le_u32_e32 vcc, 4, v11
	s_mov_b64 s[18:19], vcc
	s_mov_b64 exec, vcc
	ds_read2_b32 v[12:13], v10 offset1:1
	ds_read2_b32 v[14:15], v10 offset0:2 offset1:3
	v_add_u32_e32 v10, 16, v10
	v_subrev_u32_e32 v11, 4, v11
	s_mov_b64 exec, s[16:17]
	v_cmp_le_u32_e32 vcc, 1, v11
	s_mov_b64 s[20:21], vcc
	v_cmp_le_u32_e32 vcc, 2, v11
	s_mov_b64 s[22:23], vcc
	v_cmp_le_u32_e32 vcc, 3, v11
	s_mov_b64 s[24:25], vcc
	s_mov_b64 exec, s[20:21]
	ds_read_b32 v16, v10
	s_mov_b64 exec, s[22:23]
	ds_read_b32 v17, v10 offset:4
	s_mov_b64 exec, s[24:25]
	ds_read_b32 v18, v10 offset:8
	s_mov_b64 exec, s[16:17]
	s_waitcnt lgkmcnt(0)
	v_lshl_or_b32 v12, v12, 5, v9
	v_lshl_or_b32 v13, v13, 5, v9
	v_lshl_or_b32 v14, v14, 5, v9
	v_lshl_or_b32 v15, v15, 5, v9
	v_lshl_or_b32 v16, v16, 5, v9
	v_lshl_or_b32 v17, v17, 5, v9
	v_lshl_or_b32 v18, v18, 5, v9
	s_mov_b64 exec, s[18:19]
	global_load_dwordx4 v[64:67], v12, s[8:9]
	global_load_dwordx4 v[68:71], v13, s[8:9]
	global_load_dwordx4 v[72:75], v14, s[8:9]
	global_load_dwordx4 v[76:79], v15, s[8:9]
	s_mov_b64 exec, s[20:21]
	global_load_dwordx4 v[80:83], v16, s[8:9]
	s_mov_b64 exec, s[22:23]
	global_load_dwordx4 v[84:87], v17, s[8:9]
	s_mov_b64 exec, s[24:25]
	global_load_dwordx4 v[88:91], v18, s[8:9]
	s_mov_b64 exec, s[12:13]
	s_waitcnt vmcnt(13)
	v_pk_add_f16 v32, v32, v36
	v_pk_add_f16 v33, v33, v37
	v_pk_add_f16 v34, v34, v38
	v_pk_add_f16 v35, v35, v39
	v_fma_mix_f32 v0, v32, 1.0, v0 op_sel_hi:[1,0,0]
	v_fma_mix_f32 v1, v32, 1.0, v1 op_sel:[1,0,0] op_sel_hi:[1,0,0]
	v_fma_mix_f32 v2, v33, 1.0, v2 op_sel_hi:[1,0,0]
	v_fma_mix_f32 v3, v33, 1.0, v3 op_sel:[1,0,0] op_sel_hi:[1,0,0]
	v_fma_mix_f32 v4, v34, 1.0, v4 op_sel_hi:[1,0,0]
	v_fma_mix_f32 v5, v34, 1.0, v5 op_sel:[1,0,0] op_sel_hi:[1,0,0]
	v_fma_mix_f32 v6, v35, 1.0, v6 op_sel_hi:[1,0,0]
	v_fma_mix_f32 v7, v35, 1.0, v7 op_sel:[1,0,0] op_sel_hi:[1,0,0]
	s_waitcnt vmcnt(11)
	v_pk_add_f16 v40, v40, v44
	v_pk_add_f16 v41, v41, v45
	v_pk_add_f16 v42, v42, v46
	v_pk_add_f16 v43, v43, v47
	v_fma_mix_f32 v0, v40, 1.0, v0 op_sel_hi:[1,0,0]
	v_fma_mix_f32 v1, v40, 1.0, v1 op_sel:[1,0,0] op_sel_hi:[1,0,0]
	v_fma_mix_f32 v2, v41, 1.0, v2 op_sel_hi:[1,0,0]
	v_fma_mix_f32 v3, v41, 1.0, v3 op_sel:[1,0,0] op_sel_hi:[1,0,0]
	v_fma_mix_f32 v4, v42, 1.0, v4 op_sel_hi:[1,0,0]
	v_fma_mix_f32 v5, v42, 1.0, v5 op_sel:[1,0,0] op_sel_hi:[1,0,0]
	v_fma_mix_f32 v6, v43, 1.0, v6 op_sel_hi:[1,0,0]
	v_fma_mix_f32 v7, v43, 1.0, v7 op_sel:[1,0,0] op_sel_hi:[1,0,0]
	s_waitcnt vmcnt(9)
	v_pk_add_f16 v48, v48, v52
	v_pk_add_f16 v49, v49, v53
	v_pk_add_f16 v50, v50, v54
	v_pk_add_f16 v51, v51, v55
	v_fma_mix_f32 v0, v48, 1.0, v0 op_sel_hi:[1,0,0]
	v_fma_mix_f32 v1, v48, 1.0, v1 op_sel:[1,0,0] op_sel_hi:[1,0,0]
	v_fma_mix_f32 v2, v49, 1.0, v2 op_sel_hi:[1,0,0]
	v_fma_mix_f32 v3, v49, 1.0, v3 op_sel:[1,0,0] op_sel_hi:[1,0,0]
	v_fma_mix_f32 v4, v50, 1.0, v4 op_sel_hi:[1,0,0]
	v_fma_mix_f32 v5, v50, 1.0, v5 op_sel:[1,0,0] op_sel_hi:[1,0,0]
	v_fma_mix_f32 v6, v51, 1.0, v6 op_sel_hi:[1,0,0]
	v_fma_mix_f32 v7, v51, 1.0, v7 op_sel:[1,0,0] op_sel_hi:[1,0,0]
	s_waitcnt vmcnt(7)
	v_pk_add_f16 v56, v56, v60
	v_pk_add_f16 v57, v57, v61
	v_pk_add_f16 v58, v58, v62
	v_pk_add_f16 v59, v59, v63
	v_fma_mix_f32 v0, v56, 1.0, v0 op_sel_hi:[1,0,0]
	v_fma_mix_f32 v1, v56, 1.0, v1 op_sel:[1,0,0] op_sel_hi:[1,0,0]
	v_fma_mix_f32 v2, v57, 1.0, v2 op_sel_hi:[1,0,0]
	v_fma_mix_f32 v3, v57, 1.0, v3 op_sel:[1,0,0] op_sel_hi:[1,0,0]
	v_fma_mix_f32 v4, v58, 1.0, v4 op_sel_hi:[1,0,0]
	v_fma_mix_f32 v5, v58, 1.0, v5 op_sel:[1,0,0] op_sel_hi:[1,0,0]
	v_fma_mix_f32 v6, v59, 1.0, v6 op_sel_hi:[1,0,0]
	v_fma_mix_f32 v7, v59, 1.0, v7 op_sel:[1,0,0] op_sel_hi:[1,0,0]
	s_mov_b64 exec, s[18:19]
	s_waitcnt vmcnt(5)
	v_pk_add_f16 v64, v64, v68
	v_pk_add_f16 v65, v65, v69
	v_pk_add_f16 v66, v66, v70
	v_pk_add_f16 v67, v67, v71
	v_fma_mix_f32 v0, v64, 1.0, v0 op_sel_hi:[1,0,0]
	v_fma_mix_f32 v1, v64, 1.0, v1 op_sel:[1,0,0] op_sel_hi:[1,0,0]
	v_fma_mix_f32 v2, v65, 1.0, v2 op_sel_hi:[1,0,0]
	v_fma_mix_f32 v3, v65, 1.0, v3 op_sel:[1,0,0] op_sel_hi:[1,0,0]
	v_fma_mix_f32 v4, v66, 1.0, v4 op_sel_hi:[1,0,0]
	v_fma_mix_f32 v5, v66, 1.0, v5 op_sel:[1,0,0] op_sel_hi:[1,0,0]
	v_fma_mix_f32 v6, v67, 1.0, v6 op_sel_hi:[1,0,0]
	v_fma_mix_f32 v7, v67, 1.0, v7 op_sel:[1,0,0] op_sel_hi:[1,0,0]
	s_waitcnt vmcnt(3)
	v_pk_add_f16 v72, v72, v76
	v_pk_add_f16 v73, v73, v77
	v_pk_add_f16 v74, v74, v78
	v_pk_add_f16 v75, v75, v79
	v_fma_mix_f32 v0, v72, 1.0, v0 op_sel_hi:[1,0,0]
	v_fma_mix_f32 v1, v72, 1.0, v1 op_sel:[1,0,0] op_sel_hi:[1,0,0]
	v_fma_mix_f32 v2, v73, 1.0, v2 op_sel_hi:[1,0,0]
	v_fma_mix_f32 v3, v73, 1.0, v3 op_sel:[1,0,0] op_sel_hi:[1,0,0]
	v_fma_mix_f32 v4, v74, 1.0, v4 op_sel_hi:[1,0,0]
	v_fma_mix_f32 v5, v74, 1.0, v5 op_sel:[1,0,0] op_sel_hi:[1,0,0]
	v_fma_mix_f32 v6, v75, 1.0, v6 op_sel_hi:[1,0,0]
	v_fma_mix_f32 v7, v75, 1.0, v7 op_sel:[1,0,0] op_sel_hi:[1,0,0]
	s_mov_b64 exec, s[20:21]
	s_waitcnt vmcnt(2)
	v_fma_mix_f32 v0, v80, 1.0, v0 op_sel_hi:[1,0,0]
	v_fma_mix_f32 v1, v80, 1.0, v1 op_sel:[1,0,0] op_sel_hi:[1,0,0]
	v_fma_mix_f32 v2, v81, 1.0, v2 op_sel_hi:[1,0,0]
	v_fma_mix_f32 v3, v81, 1.0, v3 op_sel:[1,0,0] op_sel_hi:[1,0,0]
	v_fma_mix_f32 v4, v82, 1.0, v4 op_sel_hi:[1,0,0]
	v_fma_mix_f32 v5, v82, 1.0, v5 op_sel:[1,0,0] op_sel_hi:[1,0,0]
	v_fma_mix_f32 v6, v83, 1.0, v6 op_sel_hi:[1,0,0]
	v_fma_mix_f32 v7, v83, 1.0, v7 op_sel:[1,0,0] op_sel_hi:[1,0,0]
	s_mov_b64 exec, s[22:23]
	s_waitcnt vmcnt(1)
	v_fma_mix_f32 v0, v84, 1.0, v0 op_sel_hi:[1,0,0]
	v_fma_mix_f32 v1, v84, 1.0, v1 op_sel:[1,0,0] op_sel_hi:[1,0,0]
	v_fma_mix_f32 v2, v85, 1.0, v2 op_sel_hi:[1,0,0]
	v_fma_mix_f32 v3, v85, 1.0, v3 op_sel:[1,0,0] op_sel_hi:[1,0,0]
	v_fma_mix_f32 v4, v86, 1.0, v4 op_sel_hi:[1,0,0]
	v_fma_mix_f32 v5, v86, 1.0, v5 op_sel:[1,0,0] op_sel_hi:[1,0,0]
	v_fma_mix_f32 v6, v87, 1.0, v6 op_sel_hi:[1,0,0]
	v_fma_mix_f32 v7, v87, 1.0, v7 op_sel:[1,0,0] op_sel_hi:[1,0,0]
	s_mov_b64 exec, s[24:25]
	s_waitcnt vmcnt(0)
	v_fma_mix_f32 v0, v88, 1.0, v0 op_sel_hi:[1,0,0]
	v_fma_mix_f32 v1, v88, 1.0, v1 op_sel:[1,0,0] op_sel_hi:[1,0,0]
	v_fma_mix_f32 v2, v89, 1.0, v2 op_sel_hi:[1,0,0]
	v_fma_mix_f32 v3, v89, 1.0, v3 op_sel:[1,0,0] op_sel_hi:[1,0,0]
	v_fma_mix_f32 v4, v90, 1.0, v4 op_sel_hi:[1,0,0]
	v_fma_mix_f32 v5, v90, 1.0, v5 op_sel:[1,0,0] op_sel_hi:[1,0,0]
	v_fma_mix_f32 v6, v91, 1.0, v6 op_sel_hi:[1,0,0]
	v_fma_mix_f32 v7, v91, 1.0, v7 op_sel:[1,0,0] op_sel_hi:[1,0,0]
	s_mov_b64 exec, s[16:17]
	s_branch .Lk3_fin
.Lk3_drainB:
	s_mov_b64 exec, s[16:17]
	v_cmp_le_u32_e32 vcc, 4, v11
	s_mov_b64 s[18:19], vcc
	s_mov_b64 exec, vcc
	ds_read2_b32 v[12:13], v10 offset1:1
	ds_read2_b32 v[14:15], v10 offset0:2 offset1:3
	v_add_u32_e32 v10, 16, v10
	v_subrev_u32_e32 v11, 4, v11
	s_mov_b64 exec, s[16:17]
	v_cmp_le_u32_e32 vcc, 1, v11
	s_mov_b64 s[20:21], vcc
	v_cmp_le_u32_e32 vcc, 2, v11
	s_mov_b64 s[22:23], vcc
	v_cmp_le_u32_e32 vcc, 3, v11
	s_mov_b64 s[24:25], vcc
	s_mov_b64 exec, s[20:21]
	ds_read_b32 v16, v10
	s_mov_b64 exec, s[22:23]
	ds_read_b32 v17, v10 offset:4
	s_mov_b64 exec, s[24:25]
	ds_read_b32 v18, v10 offset:8
	s_mov_b64 exec, s[16:17]
	s_waitcnt lgkmcnt(0)
	v_lshl_or_b32 v12, v12, 5, v9
	v_lshl_or_b32 v13, v13, 5, v9
	v_lshl_or_b32 v14, v14, 5, v9
	v_lshl_or_b32 v15, v15, 5, v9
	v_lshl_or_b32 v16, v16, 5, v9
	v_lshl_or_b32 v17, v17, 5, v9
	v_lshl_or_b32 v18, v18, 5, v9
	s_mov_b64 exec, s[18:19]
	global_load_dwordx4 v[32:35], v12, s[8:9]
	global_load_dwordx4 v[36:39], v13, s[8:9]
	global_load_dwordx4 v[40:43], v14, s[8:9]
	global_load_dwordx4 v[44:47], v15, s[8:9]
	s_mov_b64 exec, s[20:21]
	global_load_dwordx4 v[48:51], v16, s[8:9]
	s_mov_b64 exec, s[22:23]
	global_load_dwordx4 v[52:55], v17, s[8:9]
	s_mov_b64 exec, s[24:25]
	global_load_dwordx4 v[56:59], v18, s[8:9]
	s_mov_b64 exec, s[14:15]
	s_waitcnt vmcnt(13)
	v_pk_add_f16 v64, v64, v68
	v_pk_add_f16 v65, v65, v69
	v_pk_add_f16 v66, v66, v70
	v_pk_add_f16 v67, v67, v71
	v_fma_mix_f32 v0, v64, 1.0, v0 op_sel_hi:[1,0,0]
	v_fma_mix_f32 v1, v64, 1.0, v1 op_sel:[1,0,0] op_sel_hi:[1,0,0]
	v_fma_mix_f32 v2, v65, 1.0, v2 op_sel_hi:[1,0,0]
	v_fma_mix_f32 v3, v65, 1.0, v3 op_sel:[1,0,0] op_sel_hi:[1,0,0]
	v_fma_mix_f32 v4, v66, 1.0, v4 op_sel_hi:[1,0,0]
	v_fma_mix_f32 v5, v66, 1.0, v5 op_sel:[1,0,0] op_sel_hi:[1,0,0]
	v_fma_mix_f32 v6, v67, 1.0, v6 op_sel_hi:[1,0,0]
	v_fma_mix_f32 v7, v67, 1.0, v7 op_sel:[1,0,0] op_sel_hi:[1,0,0]
	s_waitcnt vmcnt(11)
	v_pk_add_f16 v72, v72, v76
	v_pk_add_f16 v73, v73, v77
	v_pk_add_f16 v74, v74, v78
	v_pk_add_f16 v75, v75, v79
	v_fma_mix_f32 v0, v72, 1.0, v0 op_sel_hi:[1,0,0]
	v_fma_mix_f32 v1, v72, 1.0, v1 op_sel:[1,0,0] op_sel_hi:[1,0,0]
	v_fma_mix_f32 v2, v73, 1.0, v2 op_sel_hi:[1,0,0]
	v_fma_mix_f32 v3, v73, 1.0, v3 op_sel:[1,0,0] op_sel_hi:[1,0,0]
	v_fma_mix_f32 v4, v74, 1.0, v4 op_sel_hi:[1,0,0]
	v_fma_mix_f32 v5, v74, 1.0, v5 op_sel:[1,0,0] op_sel_hi:[1,0,0]
	v_fma_mix_f32 v6, v75, 1.0, v6 op_sel_hi:[1,0,0]
	v_fma_mix_f32 v7, v75, 1.0, v7 op_sel:[1,0,0] op_sel_hi:[1,0,0]
	s_waitcnt vmcnt(9)
	v_pk_add_f16 v80, v80, v84
	v_pk_add_f16 v81, v81, v85
	v_pk_add_f16 v82, v82, v86
	v_pk_add_f16 v83, v83, v87
	v_fma_mix_f32 v0, v80, 1.0, v0 op_sel_hi:[1,0,0]
	v_fma_mix_f32 v1, v80, 1.0, v1 op_sel:[1,0,0] op_sel_hi:[1,0,0]
	v_fma_mix_f32 v2, v81, 1.0, v2 op_sel_hi:[1,0,0]
	v_fma_mix_f32 v3, v81, 1.0, v3 op_sel:[1,0,0] op_sel_hi:[1,0,0]
	v_fma_mix_f32 v4, v82, 1.0, v4 op_sel_hi:[1,0,0]
	v_fma_mix_f32 v5, v82, 1.0, v5 op_sel:[1,0,0] op_sel_hi:[1,0,0]
	v_fma_mix_f32 v6, v83, 1.0, v6 op_sel_hi:[1,0,0]
	v_fma_mix_f32 v7, v83, 1.0, v7 op_sel:[1,0,0] op_sel_hi:[1,0,0]
	s_waitcnt vmcnt(7)
	v_pk_add_f16 v88, v88, v92
	v_pk_add_f16 v89, v89, v93
	v_pk_add_f16 v90, v90, v94
	v_pk_add_f16 v91, v91, v95
	v_fma_mix_f32 v0, v88, 1.0, v0 op_sel_hi:[1,0,0]
	v_fma_mix_f32 v1, v88, 1.0, v1 op_sel:[1,0,0] op_sel_hi:[1,0,0]
	v_fma_mix_f32 v2, v89, 1.0, v2 op_sel_hi:[1,0,0]
	v_fma_mix_f32 v3, v89, 1.0, v3 op_sel:[1,0,0] op_sel_hi:[1,0,0]
	v_fma_mix_f32 v4, v90, 1.0, v4 op_sel_hi:[1,0,0]
	v_fma_mix_f32 v5, v90, 1.0, v5 op_sel:[1,0,0] op_sel_hi:[1,0,0]
	v_fma_mix_f32 v6, v91, 1.0, v6 op_sel_hi:[1,0,0]
	v_fma_mix_f32 v7, v91, 1.0, v7 op_sel:[1,0,0] op_sel_hi:[1,0,0]
	s_mov_b64 exec, s[18:19]
	s_waitcnt vmcnt(5)
	v_pk_add_f16 v32, v32, v36
	v_pk_add_f16 v33, v33, v37
	v_pk_add_f16 v34, v34, v38
	v_pk_add_f16 v35, v35, v39
	v_fma_mix_f32 v0, v32, 1.0, v0 op_sel_hi:[1,0,0]
	v_fma_mix_f32 v1, v32, 1.0, v1 op_sel:[1,0,0] op_sel_hi:[1,0,0]
	v_fma_mix_f32 v2, v33, 1.0, v2 op_sel_hi:[1,0,0]
	v_fma_mix_f32 v3, v33, 1.0, v3 op_sel:[1,0,0] op_sel_hi:[1,0,0]
	v_fma_mix_f32 v4, v34, 1.0, v4 op_sel_hi:[1,0,0]
	v_fma_mix_f32 v5, v34, 1.0, v5 op_sel:[1,0,0] op_sel_hi:[1,0,0]
	v_fma_mix_f32 v6, v35, 1.0, v6 op_sel_hi:[1,0,0]
	v_fma_mix_f32 v7, v35, 1.0, v7 op_sel:[1,0,0] op_sel_hi:[1,0,0]
	s_waitcnt vmcnt(3)
	v_pk_add_f16 v40, v40, v44
	v_pk_add_f16 v41, v41, v45
	v_pk_add_f16 v42, v42, v46
	v_pk_add_f16 v43, v43, v47
	v_fma_mix_f32 v0, v40, 1.0, v0 op_sel_hi:[1,0,0]
	v_fma_mix_f32 v1, v40, 1.0, v1 op_sel:[1,0,0] op_sel_hi:[1,0,0]
	v_fma_mix_f32 v2, v41, 1.0, v2 op_sel_hi:[1,0,0]
	v_fma_mix_f32 v3, v41, 1.0, v3 op_sel:[1,0,0] op_sel_hi:[1,0,0]
	v_fma_mix_f32 v4, v42, 1.0, v4 op_sel_hi:[1,0,0]
	v_fma_mix_f32 v5, v42, 1.0, v5 op_sel:[1,0,0] op_sel_hi:[1,0,0]
	v_fma_mix_f32 v6, v43, 1.0, v6 op_sel_hi:[1,0,0]
	v_fma_mix_f32 v7, v43, 1.0, v7 op_sel:[1,0,0] op_sel_hi:[1,0,0]
	s_mov_b64 exec, s[20:21]
	s_waitcnt vmcnt(2)
	v_fma_mix_f32 v0, v48, 1.0, v0 op_sel_hi:[1,0,0]
	v_fma_mix_f32 v1, v48, 1.0, v1 op_sel:[1,0,0] op_sel_hi:[1,0,0]
	v_fma_mix_f32 v2, v49, 1.0, v2 op_sel_hi:[1,0,0]
	v_fma_mix_f32 v3, v49, 1.0, v3 op_sel:[1,0,0] op_sel_hi:[1,0,0]
	v_fma_mix_f32 v4, v50, 1.0, v4 op_sel_hi:[1,0,0]
	v_fma_mix_f32 v5, v50, 1.0, v5 op_sel:[1,0,0] op_sel_hi:[1,0,0]
	v_fma_mix_f32 v6, v51, 1.0, v6 op_sel_hi:[1,0,0]
	v_fma_mix_f32 v7, v51, 1.0, v7 op_sel:[1,0,0] op_sel_hi:[1,0,0]
	s_mov_b64 exec, s[22:23]
	s_waitcnt vmcnt(1)
	v_fma_mix_f32 v0, v52, 1.0, v0 op_sel_hi:[1,0,0]
	v_fma_mix_f32 v1, v52, 1.0, v1 op_sel:[1,0,0] op_sel_hi:[1,0,0]
	v_fma_mix_f32 v2, v53, 1.0, v2 op_sel_hi:[1,0,0]
	v_fma_mix_f32 v3, v53, 1.0, v3 op_sel:[1,0,0] op_sel_hi:[1,0,0]
	v_fma_mix_f32 v4, v54, 1.0, v4 op_sel_hi:[1,0,0]
	v_fma_mix_f32 v5, v54, 1.0, v5 op_sel:[1,0,0] op_sel_hi:[1,0,0]
	v_fma_mix_f32 v6, v55, 1.0, v6 op_sel_hi:[1,0,0]
	v_fma_mix_f32 v7, v55, 1.0, v7 op_sel:[1,0,0] op_sel_hi:[1,0,0]
	s_mov_b64 exec, s[24:25]
	s_waitcnt vmcnt(0)
	v_fma_mix_f32 v0, v56, 1.0, v0 op_sel_hi:[1,0,0]
	v_fma_mix_f32 v1, v56, 1.0, v1 op_sel:[1,0,0] op_sel_hi:[1,0,0]
	v_fma_mix_f32 v2, v57, 1.0, v2 op_sel_hi:[1,0,0]
	v_fma_mix_f32 v3, v57, 1.0, v3 op_sel:[1,0,0] op_sel_hi:[1,0,0]
	v_fma_mix_f32 v4, v58, 1.0, v4 op_sel_hi:[1,0,0]
	v_fma_mix_f32 v5, v58, 1.0, v5 op_sel:[1,0,0] op_sel_hi:[1,0,0]
	v_fma_mix_f32 v6, v59, 1.0, v6 op_sel_hi:[1,0,0]
	v_fma_mix_f32 v7, v59, 1.0, v7 op_sel:[1,0,0] op_sel_hi:[1,0,0]
	s_mov_b64 exec, s[16:17]
	s_branch .Lk3_fin
.Lk3_fin:
	v_mov_b64_e32 v[8:9], v[0:1]
	v_mov_b64_e32 v[10:11], v[2:3]
	v_mov_b64_e32 v[12:13], v[4:5]
	v_mov_b64_e32 v[14:15], v[6:7]

	.amdhsa_kernel _Z8k_layer1PKiS0_PKfPK6__halfS2_S2_P7__half2
		.amdhsa_group_segment_fixed_size 6272
		.amdhsa_private_segment_fixed_size 0
		.amdhsa_kernarg_size 56
		.amdhsa_user_sgpr_count 2
		.amdhsa_user_sgpr_dispatch_ptr 0
		.amdhsa_user_sgpr_queue_ptr 0
		.amdhsa_user_sgpr_kernarg_segment_ptr 1
		.amdhsa_user_sgpr_dispatch_id 0
		.amdhsa_user_sgpr_kernarg_preload_length 0
		.amdhsa_user_sgpr_kernarg_preload_offset 0
		.amdhsa_user_sgpr_private_segment_size 0
		.amdhsa_uses_dynamic_stack 0
		.amdhsa_enable_private_segment 0
		.amdhsa_system_sgpr_workgroup_id_x 1
		.amdhsa_system_sgpr_workgroup_id_y 0
		.amdhsa_system_sgpr_workgroup_id_z 0
		.amdhsa_system_sgpr_workgroup_info 0
		.amdhsa_system_vgpr_workitem_id 0
		.amdhsa_next_free_vgpr 96
		.amdhsa_next_free_sgpr 75
		.amdhsa_accum_offset 96
		.amdhsa_reserve_vcc 1
		.amdhsa_float_round_mode_32 0
		.amdhsa_float_round_mode_16_64 0
		.amdhsa_float_denorm_mode_32 3
		.amdhsa_float_denorm_mode_16_64 3
		.amdhsa_dx10_clamp 1
		.amdhsa_ieee_mode 1
		.amdhsa_fp16_overflow 0
		.amdhsa_tg_split 0
		.amdhsa_exception_fp_ieee_invalid_op 0
		.amdhsa_exception_fp_denorm_src 0
		.amdhsa_exception_fp_ieee_div_zero 0
		.amdhsa_exception_fp_ieee_overflow 0
		.amdhsa_exception_fp_ieee_underflow 0
		.amdhsa_exception_fp_ieee_inexact 0
		.amdhsa_exception_int_div_zero 0
	.end_amdhsa_kernel

.Lfunc_end2:
	.size	_Z8k_layer1PKiS0_PKfPK6__halfS2_S2_P7__half2, .Lfunc_end2-_Z8k_layer1PKiS0_PKfPK6__halfS2_S2_P7__half2
	.set _Z8k_layer1PKiS0_PKfPK6__halfS2_S2_P7__half2.num_vgpr, 96
	.set _Z8k_layer1PKiS0_PKfPK6__halfS2_S2_P7__half2.num_agpr, 0
	.set _Z8k_layer1PKiS0_PKfPK6__halfS2_S2_P7__half2.numbered_sgpr, 16
	.set _Z8k_layer1PKiS0_PKfPK6__halfS2_S2_P7__half2.num_named_barrier, 0
	.set _Z8k_layer1PKiS0_PKfPK6__halfS2_S2_P7__half2.private_seg_size, 0
	.set _Z8k_layer1PKiS0_PKfPK6__halfS2_S2_P7__half2.uses_vcc, 1
	.set _Z8k_layer1PKiS0_PKfPK6__halfS2_S2_P7__half2.uses_flat_scratch, 0
	.set _Z8k_layer1PKiS0_PKfPK6__halfS2_S2_P7__half2.has_dyn_sized_stack, 0
	.set _Z8k_layer1PKiS0_PKfPK6__halfS2_S2_P7__half2.has_recursion, 0
	.set _Z8k_layer1PKiS0_PKfPK6__halfS2_S2_P7__half2.has_indirect_call, 0

amdhsa.kernels:
  - .agpr_count:     0
    .args:
      - .actual_access:  read_only
        .address_space:  global
        .offset:         0
        .size:           8
        .value_kind:     global_buffer
      - .actual_access:  read_only
        .address_space:  global
        .offset:         8
        .size:           8
        .value_kind:     global_buffer
      - .actual_access:  write_only
        .address_space:  global
        .offset:         16
        .size:           8
        .value_kind:     global_buffer
      - .actual_access:  write_only
        .address_space:  global
        .offset:         24
        .size:           8
        .value_kind:     global_buffer
      - .actual_access:  read_only
        .address_space:  global
        .offset:         32
        .size:           8
        .value_kind:     global_buffer
      - .actual_access:  read_only
        .address_space:  global
        .offset:         40
        .size:           8
        .value_kind:     global_buffer
      - .actual_access:  read_only
        .address_space:  global
        .offset:         48
        .size:           8
        .value_kind:     global_buffer
      - .actual_access:  read_only
        .address_space:  global
        .offset:         56
        .size:           8
        .value_kind:     global_buffer
      - .actual_access:  write_only
        .address_space:  global
        .offset:         64
        .size:           8
        .value_kind:     global_buffer
      - .actual_access:  read_only
        .address_space:  global
        .offset:         72
        .size:           8
        .value_kind:     global_buffer
      - .actual_access:  write_only
        .address_space:  global
        .offset:         80
        .size:           8
        .value_kind:     global_buffer
    .group_segment_fixed_size: 55632
    .kernarg_segment_align: 8
    .kernarg_segment_size: 88
    .language:       OpenCL C
    .language_version:
      - 2
      - 0
    .max_flat_workgroup_size: 1024
    .name:           _Z9k_scatterPKiS0_PiPjPKfS4_S4_S4_PfS4_PDv4_j
    .private_segment_fixed_size: 0
    .sgpr_count:     58
    .sgpr_spill_count: 0
    .symbol:         _Z9k_scatterPKiS0_PiPjPKfS4_S4_S4_PfS4_PDv4_j.kd
    .uniform_work_group_size: 1
    .uses_dynamic_stack: false
    .vgpr_count:     114
    .vgpr_spill_count: 0
    .wavefront_size: 64
  - .agpr_count:     0
    .args:
      - .actual_access:  read_only
        .address_space:  global
        .offset:         0
        .size:           8
        .value_kind:     global_buffer
      - .actual_access:  read_only
        .address_space:  global
        .offset:         8
        .size:           8
        .value_kind:     global_buffer
      - .actual_access:  read_only
        .address_space:  global
        .offset:         16
        .size:           8
        .value_kind:     global_buffer
      - .actual_access:  read_only
        .address_space:  global
        .offset:         24
        .size:           8
        .value_kind:     global_buffer
      - .actual_access:  write_only
        .address_space:  global
        .offset:         32
        .size:           8
        .value_kind:     global_buffer
      - .actual_access:  write_only
        .address_space:  global
        .offset:         40
        .size:           8
        .value_kind:     global_buffer
      - .actual_access:  write_only
        .address_space:  global
        .offset:         48
        .size:           8
        .value_kind:     global_buffer
      - .actual_access:  write_only
        .address_space:  global
        .offset:         56
        .size:           8
        .value_kind:     global_buffer
    .group_segment_fixed_size: 37232
    .kernarg_segment_align: 8
    .kernarg_segment_size: 64
    .language:       OpenCL C
    .language_version:
      - 2
      - 0
    .max_flat_workgroup_size: 256
    .name:           _Z9k_binsortPKjPKiPKfPKDv4_jPiS8_PfP6__half
    .private_segment_fixed_size: 0
    .sgpr_count:     104
    .sgpr_spill_count: 0
    .symbol:         _Z9k_binsortPKjPKiPKfPKDv4_jPiS8_PfP6__half.kd
    .uniform_work_group_size: 1
    .uses_dynamic_stack: false
    .vgpr_count:     168
    .vgpr_spill_count: 0
    .wavefront_size: 64
  - .agpr_count:     0
    .args:
      - .actual_access:  read_only
        .address_space:  global
        .offset:         0
        .size:           8
        .value_kind:     global_buffer
      - .actual_access:  read_only
        .address_space:  global
        .offset:         8
        .size:           8
        .value_kind:     global_buffer
      - .actual_access:  read_only
        .address_space:  global
        .offset:         16
        .size:           8
        .value_kind:     global_buffer
      - .actual_access:  read_only
        .address_space:  global
        .offset:         24
        .size:           8
        .value_kind:     global_buffer
      - .actual_access:  read_only
        .address_space:  global
        .offset:         32
        .size:           8
        .value_kind:     global_buffer
      - .actual_access:  read_only
        .address_space:  global
        .offset:         40
        .size:           8
        .value_kind:     global_buffer
      - .actual_access:  write_only
        .address_space:  global
        .offset:         48
        .size:           8
        .value_kind:     global_buffer
    .group_segment_fixed_size: 6272
    .kernarg_segment_align: 8
    .kernarg_segment_size: 56
    .language:       OpenCL C
    .language_version:
      - 2
      - 0
    .max_flat_workgroup_size: 64
    .name:           _Z8k_layer1PKiS0_PKfPK6__halfS2_S2_P7__half2
    .private_segment_fixed_size: 0
    .sgpr_count:     22
    .sgpr_spill_count: 0
    .symbol:         _Z8k_layer1PKiS0_PKfPK6__halfS2_S2_P7__half2.kd
    .uniform_work_group_size: 1
    .uses_dynamic_stack: false
    .vgpr_count:     96
    .vgpr_spill_count: 0
    .wavefront_size: 64
  - .agpr_count:     0
    .args:
      - .actual_access:  read_only
        .address_space:  global
        .offset:         0
        .size:           8
        .value_kind:     global_buffer
      - .actual_access:  read_only
        .address_space:  global
        .offset:         8
        .size:           8
        .value_kind:     global_buffer
      - .actual_access:  read_only
        .address_space:  global
        .offset:         16
        .size:           8
        .value_kind:     global_buffer
      - .actual_access:  read_only
        .address_space:  global
        .offset:         24
        .size:           8
        .value_kind:     global_buffer
      - .actual_access:  read_only
        .address_space:  global
        .offset:         32
        .size:           8
        .value_kind:     global_buffer
      - .actual_access:  write_only
        .address_space:  global
        .offset:         40
        .size:           8
        .value_kind:     global_buffer
    .group_segment_fixed_size: 157408
    .kernarg_segment_align: 8
    .kernarg_segment_size: 48
    .language:       OpenCL C
    .language_version:
      - 2
      - 0
    .max_flat_workgroup_size: 1024
    .name:           _Z8k_layer2PKiS0_PKfPKjS2_P15HIP_vector_typeIfLj2EE
    .private_segment_fixed_size: 0
    .sgpr_count:     30
    .sgpr_spill_count: 0
    .symbol:         _Z8k_layer2PKiS0_PKfPKjS2_P15HIP_vector_typeIfLj2EE.kd
    .uniform_work_group_size: 1
    .uses_dynamic_stack: false
    .vgpr_count:     115
    .vgpr_spill_count: 0
    .wavefront_size: 64
  - .agpr_count:     0
    .args:
      - .actual_access:  read_only
        .address_space:  global
        .offset:         0
        .size:           8
        .value_kind:     global_buffer
      - .actual_access:  read_only
        .address_space:  global
        .offset:         8
        .size:           8
        .value_kind:     global_buffer
      - .actual_access:  write_only
        .address_space:  global
        .offset:         16
        .size:           8
        .value_kind:     global_buffer
    .group_segment_fixed_size: 0
    .kernarg_segment_align: 8
    .kernarg_segment_size: 24
    .language:       OpenCL C
    .language_version:
      - 2
      - 0
    .max_flat_workgroup_size: 256
    .name:           _Z5k_outPK15HIP_vector_typeIiLj4EEPKS_IfLj2EEPS3_
    .private_segment_fixed_size: 0
    .sgpr_count:     14
    .sgpr_spill_count: 0
    .symbol:         _Z5k_outPK15HIP_vector_typeIiLj4EEPKS_IfLj2EEPS3_.kd
    .uniform_work_group_size: 1
    .uses_dynamic_stack: false
    .vgpr_count:     14
    .vgpr_spill_count: 0
    .wavefront_size: 64
